# all Y-tile loads of the gate-merge epilogue made L1-bypassing (sc1); per-wave L1 invalidate between branch GEMMs and gate GEMM removed
# speedup vs baseline: 1.0333x; 1.0165x over previous
; #define PG8_LAS __attribute__((address_space(3)))
;     __host__ __device__ void init(int M, int G_, int c_) { so.init(M, 1024, G_, c_); }
;     __host__ __device__ bool next(int i, Unit& u) const { if (!so.next(i / 3, u)) return false; u.pn += 4 * (i % 3); u.idx = i; return true; }
; __device__ __forceinline__ unsigned char* launder(unsigned char* p) { asm volatile("" : "+s"(p)); return p; }
; #define IN(i) inptr(F.lds, (i))
; #define LL launder_i(l)
; #define WSP(T, off) ((T*)(launder(args.ws) + (off)))
; template <class Sched> __device__ __forceinline__ void fill_tabs_q(const float* rowfac, const float* cvec, const float* gb, const float* sbv, const Sched& S, int tid) {
;     const int c = tid & 255;
; #pragma unroll 1
;     for (int i0 = 0; i0 < 8; i0 += 4) {
;         float va[4], vb[4], vc[4]; bool ok[4];
; #pragma unroll
;         for (int j = 0; j < 4; ++j) { Unit u; ok[j] = S.next(i0 + j, u); if (!ok[j]) { u.pm = 0; u.pn = 0; }
;             if (tid < 256) va[j] = *(const g_f32*)(rowfac + u.pm * BM + c);
;             else { va[j] = *(const g_f32*)(cvec + (size_t)((u.pm * BM) / SEQ) * 4096 + u.pn * BM + c); vb[j] = *(const g_f32*)(sbv + u.pn * BM + c); vc[j] = gb ? *(const g_f32*)(gb + u.pn * BM + c) : 0.f; } }
; #pragma unroll
;         for (int j = 0; j < 4; ++j) if (ok[j]) {
;             if (tid < 256) ((PG8_LAS float*)(uintptr_t)(RSTD_LDS + (i0 + j) * 1024))[c] = va[j];
;             else { ((PG8_LAS float*)(uintptr_t)(CV_LDS + (i0 + j) * 1024))[c] = va[j] + vc[j]; ((PG8_LAS float*)(uintptr_t)(SB_LDS + (i0 + j) * 1024))[c] = vb[j]; } } }
; __global__ void __launch_bounds__(NWAVES * 64, 2) mega_fwd(Args args) {
;     ...
;         asm volatile("s_waitcnt vmcnt(0)" ::: "memory");
;         __builtin_amdgcn_fence(__ATOMIC_ACQUIRE, "agent");
;         __syncthreads();
;         }
;     ...
;         { pg8::Gemm g{(const f16*)((const unsigned char*)xout + (size_t)64 * MiB), (const f16*)(launder(args.ws) + WS_WQG + (size_t)LL * GCOLS * 1024), MTOK, GCOLS, DM / 2}; pg8::TripleOrder S; S.init(MTOK, F.G, (int)blockIdx.x);
;           pg8::EpiGateMerge<true> E{WSP(f16, WS_R1), WSP(f16, WS_R1) + 3 * YSTR};
;           pg8::fill_tabs_q((const float*)launder(args.ws) + CW_RF, WSP(float, WS_CVEC) + (size_t)(LL * 3 + 1) * 16 * 4096, IN(I_GATEB) + LL * GCOLS, WSP(float, WS_SB) + (LL * 3 + 1) * 4096, S, TID);
.LBB0_1138:
	v_readlane_b32 s50, v253, 54
	v_readlane_b32 s51, v253, 55
	s_mov_b64 s[48:49], s[50:51]
	s_mov_b32 s26, s77
	s_mov_b64 s[44:45], s[50:51]
	s_mov_b64 s[46:47], s[50:51]
	s_mov_b64 s[36:37], s[50:51]
	s_mov_b64 s[34:35], s[50:51]
	s_mov_b32 s27, s77
	s_waitcnt vmcnt(0)
	s_waitcnt vmcnt(0)
	s_nop 0
	s_barrier
	s_mul_i32 s38, s27, 3
	s_ashr_i32 s39, s38, 31
	s_lshl_b64 s[38:39], s[38:39], 18
	s_mov_b32 s27, 0x22238
	v_mov_b32 v0, s27
	s_add_u32 s27, s34, s38
	s_addc_u32 s34, s35, s39
	ds_read_b64 v[2:3], v0
	s_add_u32 s27, s27, 0x280000
	s_addc_u32 s60, s34, 0
	s_mov_b32 s34, s77
	s_mulk_i32 s34, 0xc00
	s_ashr_i32 s35, s34, 31
	s_waitcnt lgkmcnt(0)
	v_readfirstlane_b32 s40, v2
	s_lshl_b64 s[34:35], s[34:35], 2
	v_readfirstlane_b32 s41, v3
	s_add_u32 s42, s40, s34
	s_addc_u32 s43, s41, s35
	s_mov_b64 s[34:35], s[50:51]
	s_mov_b32 s38, s77
	s_mulk_i32 s38, 0x3000
	s_addk_i32 s38, 0x1000
	s_ashr_i32 s39, s38, 31
	v_mbcnt_lo_u32_b32 v0, -1, 0
	v_mbcnt_hi_u32_b32 v0, -1, v0
	s_lshl_b64 s[38:39], s[38:39], 2
	v_add_u32_e32 v0, s18, v0
	s_add_u32 s38, s34, s38
	v_and_b32_e32 v16, 0xff, v0
	s_movk_i32 s28, 0xff
	s_addc_u32 s39, s35, s39
	v_cmp_lt_i32_e64 s[34:35], s28, v0
	v_lshlrev_b32_e32 v0, 2, v16
	v_lshl_add_u64 v[2:3], s[38:39], 0, v[0:1]
	s_mov_b64 s[28:29], 0x3c0000
	v_lshl_add_u64 v[18:19], v[2:3], 0, s[28:29]
	v_lshl_add_u64 v[2:3], s[36:37], 0, v[0:1]
	s_mov_b64 s[28:29], 0x80000
	v_lshl_add_u64 v[22:23], v[2:3], 0, s[28:29]
	v_mov_b32_e32 v2, v1
	v_mov_b32_e32 v3, v1
	s_cmp_lg_u64 s[40:41], 0
	v_lshl_add_u64 v[20:21], s[42:43], 0, v[0:1]
	v_mov_b32_e32 v0, v1
	v_mov_b64_e32 v[6:7], v[2:3]
	v_mov_b64_e32 v[10:11], v[2:3]
	s_mov_b64 s[38:39], 0
	s_cselect_b64 s[50:51], -1, 0
	s_mov_b32 s61, 0
	s_mov_b64 s[36:37], -1
	v_mov_b64_e32 v[4:5], v[0:1]
	v_mov_b64_e32 v[8:9], v[0:1]
	s_branch .LBB0_1141

; #define PG8_LAS __attribute__((address_space(3)))
;     __device__ __forceinline__ void operator()(const f32x4 (&acc)[2][2][4][2], const Unit& u, int wr, int wc, int fr, int fq) const {
;         const int br = u.pn >> 2, pc = u.pn & 3;
;         const int row0 = u.pm * BM + wr * 64 + fr; const int col0 = pc * BM + wc * 32 + 8 * fq;
;         if (br == 2) { __builtin_amdgcn_fence(__ATOMIC_ACQUIRE, "agent"); }
;         const int b = (u.pm * BM) / SEQ; float rs[2][4]; row_rstd(u, wr, fr, rs);
;         f32x4 bv[2][2];
; #pragma unroll
;         for (int bj = 0; bj < 2; ++bj)
; #pragma unroll
;             for (int n = 0; n < 2; ++n) bv[bj][n] = *(const PG8_LAS f32x4*)(uintptr_t)(CV_LDS + u.idx * 1024 + (wc * 32 + 8 * fq + bj * HALF + 4 * n) * 4);
;         f32x4 sv[2][2];
;         if constexpr (I8) {
; #pragma unroll
;             for (int bj = 0; bj < 2; ++bj)
; #pragma unroll
;                 for (int n = 0; n < 2; ++n) sv[bj][n] = *(const PG8_LAS f32x4*)(uintptr_t)(SB_LDS + u.idx * 1024 + (wc * 32 + 8 * fq + bj * HALF + 4 * n) * 4); }
;         f16* Yb = Y + (size_t)br * YSTR;
; #pragma unroll
;         for (int ai = 0; ai < 2; ++ai) {
;             const int rowa = row0 + ai * HALF; const size_t offa = (size_t)rowa * 1024 + (size_t)(rowa >> 12) * GAPY + col0;
; #pragma unroll
;             for (int mp = 0; mp < 2; ++mp) {
;             f16x8 yv[4][2];
; #pragma unroll
;             for (int m = 2 * mp; m < 2 * mp + 2; ++m)
; #pragma unroll
;                 for (int bj = 0; bj < 2; ++bj) yv[m][bj] = *(const g_f16x8*)(Yb + offa + (size_t)m * 16 * 1024 + bj * HALF);
.LBB0_1228:
	s_lshl_b32 s37, s47, 8
	s_and_b32 s37, s37, 0x300
	v_lshl_add_u32 v218, s26, 8, v208
	v_add_u32_e32 v216, s37, v237
	s_lshl_b32 s46, s46, 10
	s_ashr_i32 s37, s36, 31
	v_ashrrev_i32_e32 v219, 31, v218
	s_add_i32 s47, s46, s87
	s_lshl_b64 s[36:37], s[36:37], 23
	v_ashrrev_i32_e32 v217, 31, v216
	v_lshlrev_b64 v[26:27], 10, v[218:219]
	s_add_u32 s48, s40, s36
	v_ashrrev_i32_e32 v28, 12, v218
	v_lshl_add_u64 v[26:27], v[26:27], 0, v[216:217]
	s_mov_b32 s26, 0xc00000
	s_addc_u32 s49, s41, s37
	v_mad_i64_i32 v[228:229], s[36:37], v28, s26, v[26:27]
	v_lshl_add_u64 v[224:225], v[228:229], 1, s[48:49]
	v_add_co_u32_e32 v26, vcc, 0x8000, v224
	global_load_dwordx4 v[190:193], v[224:225], off sc1
	global_load_dwordx4 v[186:189], v[224:225], off offset:256 sc1
	v_addc_co_u32_e32 v27, vcc, 0, v225, vcc
	global_load_dwordx4 v[174:177], v[26:27], off sc1
	global_load_dwordx4 v[162:165], v[26:27], off offset:256 sc1
	v_lshl_add_u32 v26, v197, 2, s47
	v_add_u32_e32 v26, 0x20000, v26
	ds_read2_b32 v[226:227], v26 offset1:16
	ds_read2_b32 v[220:221], v26 offset0:32 offset1:48
	ds_read2_b32 v[214:215], v26 offset0:128 offset1:144
	ds_read2_b32 v[212:213], v26 offset0:160 offset1:176
	v_add_u32_e32 v26, s46, v199
	v_add_u32_e32 v30, s46, v244
	ds_read_b128 v[62:65], v26
	ds_read_b128 v[50:53], v26 offset:16
	ds_read_b128 v[34:37], v26 offset:512
	ds_read_b128 v[26:29], v26 offset:528
	ds_read_b128 v[70:73], v30
	ds_read_b128 v[54:57], v30 offset:16
	ds_read_b128 v[38:41], v30 offset:512
	ds_read_b128 v[30:33], v30 offset:528
	v_cndmask_b32_e64 v42, 0, 1, s[38:39]
	v_cmp_ne_u32_e64 s[36:37], 1, v42
	v_bfrev_b32_e32 v211, 1
	s_andn2_b64 vcc, exec, s[38:39]
	s_cbranch_vccnz .LBB0_1230
	v_lshlrev_b64 v[42:43], 1, v[228:229]
	v_lshl_add_u64 v[44:45], s[40:41], 0, v[42:43]
	v_lshl_add_u64 v[46:47], s[44:45], 0, v[42:43]
	global_load_dwordx4 v[58:61], v[44:45], off sc1
	s_nop 0
	global_load_dwordx4 v[42:45], v[44:45], off offset:256 sc1
	s_nop 0
	global_load_dwordx4 v[66:69], v[46:47], off sc1
	s_nop 0
	global_load_dwordx4 v[46:49], v[46:47], off offset:256 sc1
	s_branch .LBB0_1231

; __device__ __forceinline__ unsigned pk2h(float lo, float hi) { f32x2 v = {lo, hi}; f16x2 h = __builtin_convertvector(v, f16x2); return __builtin_bit_cast(unsigned, h); }
;     __device__ __forceinline__ void operator()(const f32x4 (&acc)[2][2][4][2], const Unit& u, int wr, int wc, int fr, int fq) const {
;     ...
;                 for (int bj = 0; bj < 2; ++bj) yv[m][bj] = *(const g_f16x8*)(Yb + offa + (size_t)m * 16 * 1024 + bj * HALF);
; #pragma unroll
;             for (int m = 2 * mp; m < 2 * mp + 2; ++m) { const size_t off = offa + (size_t)m * 16 * 1024;
;                 f16x8 za[2], zb[2];
;                 if (br == 2) {
; #pragma unroll
;                     for (int bj = 0; bj < 2; ++bj) { za[bj] = *(const g_f16x8*)(Y + off + bj * HALF); zb[bj] = *(const g_f16x8*)(Y + YSTR + off + bj * HALF); } }
; #pragma unroll
;                 for (int bj = 0; bj < 2; ++bj) {
;                     f32x4 a0 = acc[ai][bj][m][0], a1 = acc[ai][bj][m][1];
;                     if constexpr (I8) { const i32x4 i0 = __builtin_bit_cast(i32x4, a0), i1 = __builtin_bit_cast(i32x4, a1);
;                         a0 = (f32x4){(float)i0.x, (float)i0.y, (float)i0.z, (float)i0.w} * sv[bj][0]; a1 = (f32x4){(float)i1.x, (float)i1.y, (float)i1.z, (float)i1.w} * sv[bj][1]; }
;                     const f32x4 g0 = a0 * rs[ai][m] + bv[bj][0], g1 = a1 * rs[ai][m] + bv[bj][1];
;                     const f16x8 yy = yv[m][bj];
;                     float z[8];
; #pragma unroll
;                     for (int e = 0; e < 4; ++e) { z[e] = (float)yy[e] * __builtin_amdgcn_rcpf(1.f + __builtin_amdgcn_exp2f(-LOG2E * g0[e])); z[4 + e] = (float)yy[4 + e] * __builtin_amdgcn_rcpf(1.f + __builtin_amdgcn_exp2f(-LOG2E * g1[e])); }
;                     if (br == 2) {
; #pragma unroll
;                         for (int e = 0; e < 8; ++e) z[e] += (float)za[bj][e] + (float)zb[bj][e]; }
;                     u32x4 w; w.x = pk2h(z[0], z[1]); w.y = pk2h(z[2], z[3]); w.z = pk2h(z[4], z[5]); w.w = pk2h(z[6], z[7]);
;                     f16* dst = (br == 2) ? merged : Yb;
;                     gst16(dst + off + bj * HALF, w); } } } }
.LBB0_1234:
	v_cvt_pk_f16_f32 v192, v180, v181
	v_cvt_f32_i32_e32 v180, v172
	v_cvt_f32_i32_e32 v172, v166
	v_cvt_pk_f16_f32 v191, v182, v183
	v_cvt_f32_i32_e32 v182, v167
	v_cvt_f32_i32_e32 v170, v170
	s_waitcnt lgkmcnt(0)
	v_mul_f32_e32 v167, v30, v172
	v_fma_f32 v167, v226, v167, v26
	v_mul_f32_e32 v167, 0xbfb8aa3b, v167
	v_exp_f32_e32 v167, v167
	v_cvt_f32_i32_e32 v171, v171
	v_mul_f32_e32 v166, v38, v170
	v_fma_f32 v166, v226, v166, v34
	v_add_f32_e32 v167, 1.0, v167
	v_rcp_f32_e32 v170, v167
	v_mul_f32_e32 v167, v39, v171
	v_fma_f32 v167, v226, v167, v35
	v_mul_f32_e32 v166, 0xbfb8aa3b, v166
	v_mul_f32_e32 v167, 0xbfb8aa3b, v167
	v_exp_f32_e32 v166, v166
	v_exp_f32_e32 v167, v167
	v_mul_f32_e32 v171, v31, v182
	v_fma_f32 v171, v226, v171, v27
	v_mul_f32_e32 v171, 0xbfb8aa3b, v171
	v_add_f32_e32 v166, 1.0, v166
	v_add_f32_e32 v167, 1.0, v167
	v_exp_f32_e32 v171, v171
	v_cvt_f32_i32_e32 v181, v173
	v_rcp_f32_e32 v166, v166
	v_rcp_f32_e32 v167, v167
	s_waitcnt vmcnt(2)
	v_cvt_f32_f16_sdwa v173, v186 dst_sel:DWORD dst_unused:UNUSED_PAD src0_sel:WORD_1
	v_cvt_f32_f16_e32 v172, v186
	v_add_f32_e32 v171, 1.0, v171
	v_rcp_f32_e32 v171, v171
	v_cvt_pk_f16_f32 v190, v178, v179
	v_pk_mul_f32 v[166:167], v[166:167], v[172:173]
	v_cvt_f32_f16_sdwa v173, v188 dst_sel:DWORD dst_unused:UNUSED_PAD src0_sel:WORD_1
	v_cvt_f32_f16_e32 v172, v188
	v_cvt_pk_f16_f32 v193, v184, v185
	v_lshl_add_u64 v[178:179], v[228:229], 1, s[46:47]
	s_mov_b64 s[52:53], -1
	v_pk_mul_f32 v[170:171], v[170:171], v[172:173]
	v_mul_f32_e32 v172, v40, v180
	v_mul_f32_e32 v173, v41, v181
	v_fma_f32 v172, v226, v172, v36
	v_fma_f32 v173, v226, v173, v37
	v_mul_f32_e32 v172, 0xbfb8aa3b, v172
	v_mul_f32_e32 v173, 0xbfb8aa3b, v173
	v_exp_f32_e32 v172, v172
	v_exp_f32_e32 v173, v173
	v_cvt_f32_f16_sdwa v181, v187 dst_sel:DWORD dst_unused:UNUSED_PAD src0_sel:WORD_1
	v_cvt_f32_f16_e32 v180, v187
	v_add_f32_e32 v172, 1.0, v172
	v_add_f32_e32 v173, 1.0, v173
	v_rcp_f32_e32 v172, v172
	v_rcp_f32_e32 v173, v173
	s_andn2_b64 vcc, exec, s[50:51]
	global_store_dwordx4 v[178:179], v[190:193], off
	v_lshl_add_u64 v[222:223], v[228:229], 1, s[48:49]
	s_mov_b64 s[28:29], 0x10000
	v_lshl_add_u64 v[222:223], v[222:223], 0, s[28:29]
	global_load_dwordx4 v[238:241], v[222:223], off sc1
	global_load_dwordx4 v[246:249], v[222:223], off offset:256 sc1
	v_pk_mul_f32 v[172:173], v[172:173], v[180:181]
	v_cndmask_b32_e64 v180, 0, 1, s[50:51]
	v_cmp_ne_u32_e64 s[38:39], 1, v180
	s_cbranch_vccnz .LBB0_1236
	s_mov_b64 s[52:53], 0

;     __device__ __forceinline__ void operator()(const f32x4 (&acc)[2][2][4][2], const Unit& u, int wr, int wc, int fr, int fq) const {
;     ...
;             for (int mp = 0; mp < 2; ++mp) {
;             f16x8 yv[4][2];
; #pragma unroll
;             for (int m = 2 * mp; m < 2 * mp + 2; ++m)
; #pragma unroll
;                 for (int bj = 0; bj < 2; ++bj) yv[m][bj] = *(const g_f16x8*)(Yb + offa + (size_t)m * 16 * 1024 + bj * HALF);
; #pragma unroll
;             for (int m = 2 * mp; m < 2 * mp + 2; ++m) { const size_t off = offa + (size_t)m * 16 * 1024;
;                 f16x8 za[2], zb[2];
;                 if (br == 2) {
; #pragma unroll
;                     for (int bj = 0; bj < 2; ++bj) { za[bj] = *(const g_f16x8*)(Y + off + bj * HALF); zb[bj] = *(const g_f16x8*)(Y + YSTR + off + bj * HALF); } }
.LBB0_1247:
	s_mov_b64 s[28:29], 0x8000
	v_lshl_add_u64 v[158:159], v[178:179], 0, s[28:29]
	v_cvt_pk_f16_f32 v154, v146, v147
	v_cvt_pk_f16_f32 v155, v152, v153
	v_cvt_pk_f16_f32 v156, v150, v151
	v_cvt_pk_f16_f32 v157, v148, v149
	v_add_co_u32_e32 v146, vcc, 0x10000, v224
	global_store_dwordx4 v[158:159], v[154:157], off offset:256
	s_nop 0
	v_addc_co_u32_e32 v147, vcc, 0, v225, vcc
	v_add_co_u32_e32 v146, vcc, 0x18000, v224
	s_nop 1
	v_addc_co_u32_e32 v147, vcc, 0, v225, vcc
	global_load_dwordx4 v[150:153], v[146:147], off sc1
	s_nop 0
	global_load_dwordx4 v[146:149], v[146:147], off offset:256 sc1
	v_lshl_add_u64 v[222:223], v[228:229], 1, s[48:49]
	s_mov_b64 s[28:29], 0x40000
	v_lshl_add_u64 v[222:223], v[222:223], 0, s[28:29]
	global_load_dwordx4 v[174:177], v[222:223], off sc1
	global_load_dwordx4 v[180:183], v[222:223], off offset:256 sc1
	s_and_b64 vcc, exec, s[36:37]
	s_cbranch_vccnz .LBB0_1249
	v_mov_b64_e32 v[42:43], 0x10000
	v_lshl_add_u64 v[42:43], v[228:229], 1, v[42:43]
	v_lshl_add_u64 v[44:45], s[40:41], 0, v[42:43]
	s_waitcnt vmcnt(6)
	v_lshl_add_u64 v[46:47], s[44:45], 0, v[42:43]
	global_load_dwordx4 v[58:61], v[44:45], off sc1
	s_nop 0
	global_load_dwordx4 v[42:45], v[44:45], off offset:256 sc1
	s_nop 0
	global_load_dwordx4 v[66:69], v[46:47], off sc1
	s_nop 0
	global_load_dwordx4 v[46:49], v[46:47], off offset:256 sc1

;     __device__ __forceinline__ void operator()(const f32x4 (&acc)[2][2][4][2], const Unit& u, int wr, int wc, int fr, int fq) const {
;     ...
;             for (int mp = 0; mp < 2; ++mp) {
;             f16x8 yv[4][2];
; #pragma unroll
;             for (int m = 2 * mp; m < 2 * mp + 2; ++m)
; #pragma unroll
;                 for (int bj = 0; bj < 2; ++bj) yv[m][bj] = *(const g_f16x8*)(Yb + offa + (size_t)m * 16 * 1024 + bj * HALF);
; #pragma unroll
;             for (int m = 2 * mp; m < 2 * mp + 2; ++m) { const size_t off = offa + (size_t)m * 16 * 1024;
;                 f16x8 za[2], zb[2];
;                 if (br == 2) {
; #pragma unroll
;                     for (int bj = 0; bj < 2; ++bj) { za[bj] = *(const g_f16x8*)(Y + off + bj * HALF); zb[bj] = *(const g_f16x8*)(Y + YSTR + off + bj * HALF); } }
.LBB0_1255:
	s_mov_b64 s[28:29], 0x10000
	v_lshl_add_u64 v[142:143], v[178:179], 0, s[28:29]
	v_cvt_pk_f16_f32 v138, v130, v131
	v_cvt_pk_f16_f32 v139, v136, v137
	v_cvt_pk_f16_f32 v140, v134, v135
	v_cvt_pk_f16_f32 v141, v132, v133
	s_and_b64 vcc, exec, s[36:37]
	global_store_dwordx4 v[142:143], v[138:141], off offset:256
	v_lshl_add_u64 v[222:223], v[228:229], 1, s[48:49]
	s_mov_b64 s[28:29], 0x48000
	v_lshl_add_u64 v[222:223], v[222:223], 0, s[28:29]
	global_load_dwordx4 v[162:165], v[222:223], off sc1
	global_load_dwordx4 v[166:169], v[222:223], off offset:256 sc1
	s_cbranch_vccnz .LBB0_1257
	v_mov_b64_e32 v[42:43], 0x18000
	v_lshl_add_u64 v[42:43], v[228:229], 1, v[42:43]
	v_lshl_add_u64 v[44:45], s[40:41], 0, v[42:43]
	s_waitcnt vmcnt(4)
	v_lshl_add_u64 v[46:47], s[44:45], 0, v[42:43]
	global_load_dwordx4 v[58:61], v[44:45], off sc1
	s_nop 0
	global_load_dwordx4 v[42:45], v[44:45], off offset:256 sc1
	s_nop 0
	global_load_dwordx4 v[66:69], v[46:47], off sc1
	s_nop 0
	global_load_dwordx4 v[46:49], v[46:47], off offset:256 sc1

;     __device__ __forceinline__ void operator()(const f32x4 (&acc)[2][2][4][2], const Unit& u, int wr, int wc, int fr, int fq) const {
;     ...
;             const int rowa = row0 + ai * HALF; const size_t offa = (size_t)rowa * 1024 + (size_t)(rowa >> 12) * GAPY + col0;
; #pragma unroll
;             for (int mp = 0; mp < 2; ++mp) {
;             f16x8 yv[4][2];
; #pragma unroll
;             for (int m = 2 * mp; m < 2 * mp + 2; ++m)
; #pragma unroll
;                 for (int bj = 0; bj < 2; ++bj) yv[m][bj] = *(const g_f16x8*)(Yb + offa + (size_t)m * 16 * 1024 + bj * HALF);
; #pragma unroll
;             for (int m = 2 * mp; m < 2 * mp + 2; ++m) { const size_t off = offa + (size_t)m * 16 * 1024;
;                 f16x8 za[2], zb[2];
;                 if (br == 2) {
; #pragma unroll
;                     for (int bj = 0; bj < 2; ++bj) { za[bj] = *(const g_f16x8*)(Y + off + bj * HALF); zb[bj] = *(const g_f16x8*)(Y + YSTR + off + bj * HALF); } }
.LBB0_1263:
	v_cvt_pk_f16_f32 v122, v114, v115
	v_add_u32_e32 v114, 0x80, v218
	v_ashrrev_i32_e32 v115, 31, v114
	v_cvt_pk_f16_f32 v125, v116, v117
	v_lshlrev_b64 v[116:117], 10, v[114:115]
	v_cvt_pk_f16_f32 v124, v118, v119
	v_ashrrev_i32_e32 v118, 12, v114
	v_lshl_add_u64 v[114:115], v[116:117], 0, v[216:217]
	s_mov_b32 s26, 0xc00000
	v_mad_i64_i32 v[130:131], s[50:51], v118, s26, v[114:115]
	s_mov_b64 s[28:29], 0x18000
	v_lshl_add_u64 v[132:133], v[130:131], 1, s[48:49]
	v_lshl_add_u64 v[126:127], v[178:179], 0, s[28:29]
	v_cvt_pk_f16_f32 v123, v120, v121
	v_add_co_u32_e32 v114, vcc, 0x8000, v132
	global_store_dwordx4 v[126:127], v[122:125], off offset:256
	v_lshl_add_u64 v[222:223], v[228:229], 1, s[48:49]
	s_mov_b64 s[28:29], 0x50000
	v_lshl_add_u64 v[222:223], v[222:223], 0, s[28:29]
	global_load_dwordx4 v[146:149], v[222:223], off sc1
	global_load_dwordx4 v[150:153], v[222:223], off offset:256 sc1
	v_lshl_add_u64 v[222:223], v[228:229], 1, s[48:49]
	s_mov_b64 s[28:29], 0x58000
	v_lshl_add_u64 v[222:223], v[222:223], 0, s[28:29]
	global_load_dwordx4 v[154:157], v[222:223], off sc1
	global_load_dwordx4 v[158:161], v[222:223], off offset:256 sc1
	s_nop 0
	v_addc_co_u32_e32 v115, vcc, 0, v133, vcc
	s_nop 0
	s_and_b64 vcc, exec, s[36:37]
	s_cbranch_vccnz .LBB0_1265
	v_lshlrev_b64 v[42:43], 1, v[130:131]
	v_lshl_add_u64 v[44:45], s[40:41], 0, v[42:43]
	s_waitcnt vmcnt(6)
	v_lshl_add_u64 v[46:47], s[44:45], 0, v[42:43]
	global_load_dwordx4 v[58:61], v[44:45], off sc1
	s_nop 0
	global_load_dwordx4 v[42:45], v[44:45], off offset:256 sc1
	s_nop 0
	global_load_dwordx4 v[66:69], v[46:47], off sc1
	s_nop 0
	global_load_dwordx4 v[46:49], v[46:47], off offset:256 sc1
